# speedup vs baseline: 1.0485x; 1.0057x over previous
_Z11knrm_kernelPKfS0_PKiS2_S0_Pf:
	s_load_dwordx8 s[4:11], s[0:1], 0x0
	s_load_dwordx4 s[12:15], s[0:1], 0x20
	v_lshrrev_b32_e32 v1, 6, v0
	v_and_b32_e32 v120, 63, v0
	v_lshrrev_b32_e32 v100, 4, v0
	v_and_b32_e32 v123, 15, v0
	v_lshlrev_b32_e32 v124, 5, v1
	s_lshl_b32 s3, s2, 5
	v_lshl_or_b32 v8, s2, 8, v124
	v_or_b32_e32 v2, s3, v100
	s_movk_i32 s3, 0x4b0
	v_mul_lo_u32 v2, v2, s3
	v_mul_lo_u32 v99, v8, s3
	v_lshlrev_b32_e32 v132, 4, v120
	v_min_u32_e32 v193, 23, v120
	v_lshl_add_u32 v3, v123, 4, v2
	v_min_u32_e32 v4, 10, v123
	v_add_u32_e32 v192, v99, v132
	v_lshlrev_b32_e32 v193, 4, v193
	s_movk_i32 s27, 0x1000
	s_movk_i32 s28, 0x2000
	v_lshl_add_u32 v2, v4, 4, v2
	v_add3_u32 v193, v99, v193, s28
	s_mov_b32 s19, 0x20000
	s_mov_b32 s18, 0x4b00000
	s_waitcnt lgkmcnt(0)
	s_mov_b64 s[16:17], s[6:7]
	s_and_b32 s5, s5, 0xffff
	s_mov_b32 s6, 0x960000
	s_mov_b32 s7, s19
	s_and_b32 s17, s17, 0xffff
	buffer_load_dwordx4 v[90:93], v3, s[4:7], 0 offen nt
	buffer_load_dwordx4 v[86:89], v3, s[4:7], 0 offen offset:256 nt
	buffer_load_dwordx4 v[82:85], v3, s[4:7], 0 offen offset:512 nt
	buffer_load_dwordx4 v[78:81], v3, s[4:7], 0 offen offset:768 nt
	buffer_load_dwordx4 v[94:97], v2, s[4:7], 0 offen offset:1024 nt
	buffer_load_dwordx4 v[2:5], v192, s[16:19], 0 offen nt
	buffer_load_dwordx4 v[14:17], v192, s[16:19], 0 offen offset:1024 nt
	buffer_load_dwordx4 v[34:37], v192, s[16:19], 0 offen offset:2048 nt
	buffer_load_dwordx4 v[46:49], v192, s[16:19], 0 offen offset:3072 nt
	buffer_load_dwordx4 v[54:57], v192, s[16:19], s27 offen nt
	buffer_load_dwordx4 v[58:61], v192, s[16:19], s27 offen offset:1024 nt
	buffer_load_dwordx4 v[62:65], v192, s[16:19], s27 offen offset:2048 nt
	buffer_load_dwordx4 v[66:69], v192, s[16:19], s27 offen offset:3072 nt
	buffer_load_dwordx4 v[70:73], v192, s[16:19], s28 offen nt
	buffer_load_dwordx4 v[74:77], v193, s[16:19], 0 offen offset:1024 nt
	v_lshlrev_b32_e32 v42, 2, v0
	v_bfe_u32 v43, v0, 2, 2
	v_and_or_b32 v98, v42, 12, v43
	v_and_or_b32 v6, v98, 7, v8
	v_ashrrev_i32_e32 v7, 31, v6
	s_movk_i32 s0, 0x160
	v_lshl_add_u64 v[6:7], v[6:7], 2, s[10:11]
	v_lshrrev_b32_e32 v121, 5, v0
	v_cmp_gt_u32_e64 s[0:1], s0, v0
	global_load_dword v125, v[6:7], off
	global_load_dword v126, v[6:7], off offset:64
	global_load_dword v127, v[6:7], off offset:96
	global_load_dword v190, v[6:7], off offset:32
	v_cndmask_b32_e64 v42, 10, v121, s[0:1]
	v_lshlrev_b32_e32 v42, 2, v42
	s_lshl_b32 s3, s2, 5
	v_and_b32_e32 v122, 31, v0
	global_load_dword v118, v42, s[12:13]
	v_or_b32_e32 v42, s3, v122
	v_ashrrev_i32_e32 v43, 31, v42
	v_lshl_add_u64 v[42:43], v[42:43], 2, s[8:9]
	global_load_dword v119, v[42:43], off
	s_mov_b32 s3, 0
	v_mul_u32_u24_e32 v131, 0x2600, v1
	v_lshl_add_u32 v141, v120, 3, v131
	v_add_u32_e32 v194, 64, v120
	v_mul_u32_u24_e32 v195, 0x1b5, v194
	v_lshrrev_b32_e32 v195, 15, v195
	v_add_u32_e32 v194, v194, v195
	v_lshl_add_u32 v143, v194, 3, v131
	v_add_u32_e32 v194, 128, v120
	v_mul_u32_u24_e32 v195, 0x1b5, v194
	v_lshrrev_b32_e32 v195, 15, v195
	v_add_u32_e32 v194, v194, v195
	v_lshl_add_u32 v144, v194, 3, v131
	v_add_u32_e32 v194, 192, v120
	v_mul_u32_u24_e32 v195, 0x1b5, v194
	v_lshrrev_b32_e32 v195, 15, v195
	v_add_u32_e32 v194, v194, v195
	v_lshl_add_u32 v145, v194, 3, v131
	v_add_u32_e32 v194, 256, v120
	v_mul_u32_u24_e32 v195, 0x1b5, v194
	v_lshrrev_b32_e32 v195, 15, v195
	v_add_u32_e32 v194, v194, v195
	v_lshl_add_u32 v146, v194, 3, v131
	v_add_u32_e32 v194, 320, v120
	v_mul_u32_u24_e32 v195, 0x1b5, v194
	v_lshrrev_b32_e32 v195, 15, v195
	v_add_u32_e32 v194, v194, v195
	v_lshl_add_u32 v147, v194, 3, v131
	v_add_u32_e32 v194, 448, v120
	v_mul_u32_u24_e32 v195, 0x1b5, v194
	v_lshrrev_b32_e32 v195, 15, v195
	v_add_u32_e32 v194, v194, v195
	v_lshl_add_u32 v148, v194, 3, v131
	v_add_u32_e32 v194, 512, v120
	v_mul_u32_u24_e32 v195, 0x1b5, v194
	v_lshrrev_b32_e32 v195, 15, v195
	v_add_u32_e32 v194, v194, v195
	v_lshl_add_u32 v149, v194, 3, v131
	v_add_u32_e32 v194, 576, v120
	v_mul_u32_u24_e32 v195, 0x1b5, v194
	v_lshrrev_b32_e32 v195, 15, v195
	v_add_u32_e32 v194, v194, v195
	v_lshl_add_u32 v150, v194, 3, v131
	v_and_b32_e32 v196, 48, v120
	v_mul_u32_u24_e32 v197, 0x260, v123
	v_mul_u32_u24_e32 v198, 0x260, v98
	v_lshrrev_b32_e32 v199, 1, v120
	v_add_u32_e32 v136, v197, v196
	v_add_u32_e32 v198, v198, v131
	v_and_b32_e32 v199, 24, v199
	v_add_u32_e32 v142, v198, v196
	v_add_u32_e32 v159, v198, v199
	v_add3_u32 v160, v197, v199, 64
	v_add_u32_e32 v142, 0x4c00, v142
	v_cmp_gt_u32_e64 s[4:5], 16, v120
	s_and_saveexec_b64 s[6:7], s[4:5]
	s_movk_i32 s8, 0x260
	v_mov_b32_e32 v102, 0
	v_mad_u32_u24 v101, v120, s8, v131
	v_mov_b32_e32 v103, v102
	ds_write_b64 v101, v[102:103] offset:20056
	s_or_b64 exec, exec, s[6:7]
	v_cmp_lt_u32_e32 vcc, 10, v123
	s_waitcnt vmcnt(19)
	v_mul_f32_e32 v101, v87, v87
	v_mov_b32_e32 v106, v92
	s_waitcnt vmcnt(16)
	v_cndmask_b32_e64 v103, v97, 0, vcc
	v_cndmask_b32_e64 v102, v96, 0, vcc
	v_mov_b32_e32 v96, v91
	v_mov_b32_e32 v97, v83
	v_cndmask_b32_e64 v105, v95, 0, vcc
	v_cndmask_b32_e64 v104, v94, 0, vcc
	v_mov_b32_e32 v94, v90
	v_mov_b32_e32 v95, v82
	v_pk_mul_f32 v[96:97], v[96:97], v[96:97]
	v_mov_b32_e32 v107, v84
	v_fmac_f32_e32 v101, v86, v86
	v_pk_fma_f32 v[94:95], v[94:95], v[94:95], v[96:97]
	v_mov_b32_e32 v108, v93
	v_mov_b32_e32 v109, v85
	v_fmac_f32_e32 v101, v88, v88
	v_pk_fma_f32 v[94:95], v[106:107], v[106:107], v[94:95]
	v_fmac_f32_e32 v101, v89, v89
	v_pk_fma_f32 v[94:95], v[108:109], v[108:109], v[94:95]
	v_mov_b32_e32 v96, v79
	v_add_f32_e32 v94, v94, v101
	v_mov_b32_e32 v97, v105
	v_add_f32_e32 v101, v94, v95
	v_mov_b32_e32 v94, v78
	v_mov_b32_e32 v95, v104
	v_pk_mul_f32 v[96:97], v[96:97], v[96:97]
	s_mov_b32 s21, 0xf800000
	v_pk_fma_f32 v[94:95], v[94:95], v[94:95], v[96:97]
	v_mov_b32_e32 v96, v80
	v_mov_b32_e32 v97, v102
	v_pk_fma_f32 v[94:95], v[96:97], v[96:97], v[94:95]
	v_mov_b32_e32 v96, v81
	v_mov_b32_e32 v97, v103
	v_pk_fma_f32 v[94:95], v[96:97], v[96:97], v[94:95]
	v_mov_b32_e32 v135, 0x260
	v_add_f32_e32 v94, v101, v94
	v_add_f32_e32 v94, v94, v95
	v_mbcnt_lo_u32_b32 v95, -1, 0
	v_mbcnt_hi_u32_b32 v95, -1, v95
	v_and_b32_e32 v97, 64, v95
	v_add_u32_e32 v101, 64, v97
	s_movk_i32 s8, 0x260
	v_add_u32_e32 v137, 0x4b00, v99
	s_movk_i32 s10, 0x1b5
	v_mov_b32_e32 v99, 0x36a00
	v_mov_b32_e32 v111, 0x666c0
	v_mov_b32_e32 v113, 0x6d400
	v_mov_b32_e32 v115, 0x74140
	s_mov_b32 s20, 0xbeb17218
	s_mov_b32 s22, 0x44132d1f
	v_mov_b32_e32 v161, 0xc47a0000
	v_add_f32_dpp v96, v94, v94 quad_perm:[1,0,3,2] row_mask:0xf bank_mask:0xf
	s_nop 1
	v_add_f32_dpp v94, v96, v96 quad_perm:[2,3,0,1] row_mask:0xf bank_mask:0xf
	s_nop 1
	v_add_f32_dpp v96, v94, v94 row_half_mirror row_mask:0xf bank_mask:0xf
	s_nop 1
	v_add_f32_dpp v94, v96, v96 row_mirror row_mask:0xf bank_mask:0xf
	v_mul_f32_e32 v96, 0x4f800000, v94
	v_cmp_gt_f32_e32 vcc, s21, v94
	s_nop 1
	v_cndmask_b32_e32 v94, v94, v96, vcc
	v_sqrt_f32_e32 v96, v94
	s_nop 0
	v_add_u32_e32 v106, -1, v96
	v_fma_f32 v107, -v106, v96, v94
	v_cmp_ge_f32_e64 s[6:7], 0, v107
	v_add_u32_e32 v107, 1, v96
	s_nop 0
	v_cndmask_b32_e64 v106, v96, v106, s[6:7]
	v_fma_f32 v96, -v107, v96, v94
	v_cmp_lt_f32_e64 s[6:7], 0, v96
	s_nop 1
	v_cndmask_b32_e64 v96, v106, v107, s[6:7]
	v_mul_f32_e32 v106, 0x37800000, v96
	v_cndmask_b32_e32 v96, v96, v106, vcc
	v_cmp_class_f32_e32 vcc, v94, v135
	s_nop 1
	v_cndmask_b32_e32 v94, v96, v94, vcc
	v_add_f32_e32 v96, 0x29e12e13, v94
	v_div_scale_f32 v106, s[6:7], v96, v96, 1.0
	v_rcp_f32_e32 v107, v106
	v_mov_b32_e32 v94, 0
	v_cmp_gt_u32_e64 s[6:7], 48, v120
	v_mov_b32_e32 v116, v94
	v_fma_f32 v108, -v106, v107, 1.0
	v_fmac_f32_e32 v107, v108, v107
	v_div_scale_f32 v108, vcc, 1.0, v96, 1.0
	v_mul_f32_e32 v109, v108, v107
	v_fma_f32 v110, -v106, v109, v108
	v_fmac_f32_e32 v109, v110, v107
	v_fma_f32 v106, -v106, v109, v108
	v_div_fmas_f32 v106, v106, v107, v109
	v_div_fixup_f32 v96, v106, v96, 1.0
	v_lshlrev_b32_e32 v106, 3, v123
	v_pk_mul_f32 v[82:83], v[96:97], v[82:83] op_sel_hi:[0,1]
	v_pk_mul_f32 v[84:85], v[96:97], v[84:85] op_sel_hi:[0,1]
	v_pk_mul_f32 v[78:79], v[96:97], v[78:79] op_sel_hi:[0,1]
	v_pk_mul_f32 v[80:81], v[96:97], v[80:81] op_sel_hi:[0,1]
	v_mad_u32_u24 v100, v100, s8, v106
	v_cvt_pk_f16_f32 v82, v82, v83
	v_cvt_pk_f16_f32 v83, v84, v85
	v_cvt_pk_f16_f32 v78, v78, v79
	v_cvt_pk_f16_f32 v79, v80, v81
	ds_write2_b64 v100, v[82:83], v[78:79] offset0:32 offset1:48
	v_pk_mul_f32 v[90:91], v[96:97], v[90:91] op_sel_hi:[0,1]
	v_pk_mul_f32 v[92:93], v[96:97], v[92:93] op_sel_hi:[0,1]
	v_pk_mul_f32 v[86:87], v[96:97], v[86:87] op_sel_hi:[0,1]
	v_pk_mul_f32 v[88:89], v[96:97], v[88:89] op_sel_hi:[0,1]
	v_pk_mul_f32 v[78:79], v[96:97], v[104:105] op_sel_hi:[0,1]
	v_pk_mul_f32 v[80:81], v[96:97], v[102:103] op_sel_hi:[0,1]
	v_sub_u32_e64 v162, v123, 11 clamp
	v_cvt_pk_f16_f32 v90, v90, v91
	v_cvt_pk_f16_f32 v91, v92, v93
	v_cvt_pk_f16_f32 v86, v86, v87
	v_cvt_pk_f16_f32 v87, v88, v89
	v_cvt_pk_f16_f32 v78, v78, v79
	v_cvt_pk_f16_f32 v79, v80, v81
	v_mad_i32_i24 v162, v162, -8, v100
	ds_write2_b64 v100, v[90:91], v[86:87] offset1:16
	ds_write_b64 v162, v[78:79] offset:512
	v_cmp_gt_u32_e64 s[8:9], 24, v120
	v_mov_b32_e32 v96, 0xc604b4df
	v_mov_b32_e32 v95, v94
	v_mov_b32_e32 v98, v94
	v_mov_b32_e32 v99, v94
	v_mov_b32_e32 v100, v94
	v_mov_b32_e32 v101, v94
	v_mov_b32_e32 v102, v94
	v_mov_b32_e32 v103, v94
	v_mov_b32_e32 v104, v94
	v_mov_b32_e32 v105, v94
	v_mov_b32_e32 v106, v94
	v_mov_b32_e32 v107, v94
	v_mov_b32_e32 v108, v94
	v_mov_b32_e32 v109, v94
	v_mov_b32_e32 v110, v94
	v_mov_b32_e32 v111, v94
	v_mov_b32_e32 v112, v94
	v_mov_b32_e32 v113, v94
	v_mov_b32_e32 v114, v94
	v_mov_b32_e32 v115, v94
	v_mov_b32_e32 v117, v94
	s_waitcnt lgkmcnt(0)
	s_barrier
	s_mov_b32 s26, 0x2580
	s_mov_b32 s27, 0x3580
	s_mov_b32 s28, 0x4580
	buffer_load_dwordx4 v[6:9], v192, s[16:19], s26 offen nt
	buffer_load_dwordx4 v[10:13], v192, s[16:19], s26 offen offset:1024 nt
	buffer_load_dwordx4 v[18:21], v192, s[16:19], s26 offen offset:2048 nt
	buffer_load_dwordx4 v[22:25], v192, s[16:19], s26 offen offset:3072 nt
	buffer_load_dwordx4 v[26:29], v192, s[16:19], s27 offen nt
	buffer_load_dwordx4 v[30:33], v192, s[16:19], s27 offen offset:1024 nt
	buffer_load_dwordx4 v[38:41], v192, s[16:19], s27 offen offset:2048 nt
	buffer_load_dwordx4 v[42:45], v192, s[16:19], s27 offen offset:3072 nt
	buffer_load_dwordx4 v[50:53], v192, s[16:19], s28 offen nt
	buffer_load_dwordx4 v[186:189], v193, s[16:19], s26 offen offset:1024 nt
	s_waitcnt vmcnt(25)
	v_cvt_pk_f16_f32 v79, v4, v5
	v_cvt_pk_f16_f32 v78, v2, v3
	ds_write_b64 v141, v[78:79] offset:19456
	s_waitcnt vmcnt(24)
	v_cvt_pk_f16_f32 v79, v16, v17
	v_cvt_pk_f16_f32 v78, v14, v15
	ds_write_b64 v143, v[78:79] offset:19456
	s_waitcnt vmcnt(23)
	v_cvt_pk_f16_f32 v79, v36, v37
	v_cvt_pk_f16_f32 v78, v34, v35
	ds_write_b64 v144, v[78:79] offset:19456
	s_waitcnt vmcnt(22)
	v_cvt_pk_f16_f32 v79, v48, v49
	v_cvt_pk_f16_f32 v78, v46, v47
	ds_write_b64 v145, v[78:79] offset:19456
	s_waitcnt vmcnt(21)
	v_cvt_pk_f16_f32 v79, v56, v57
	v_cvt_pk_f16_f32 v78, v54, v55
	ds_write_b64 v146, v[78:79] offset:19456
	s_waitcnt vmcnt(20)
	v_cvt_pk_f16_f32 v79, v60, v61
	v_cvt_pk_f16_f32 v78, v58, v59
	ds_write_b64 v147, v[78:79] offset:19456
	s_waitcnt vmcnt(19)
	v_cvt_pk_f16_f32 v79, v64, v65
	v_cvt_pk_f16_f32 v78, v62, v63
	ds_write_b64 v141, v[78:79] offset:22568
	s_waitcnt vmcnt(18)
	v_cvt_pk_f16_f32 v79, v68, v69
	v_cvt_pk_f16_f32 v78, v66, v67
	ds_write_b64 v148, v[78:79] offset:19456
	s_waitcnt vmcnt(17)
	v_cvt_pk_f16_f32 v79, v72, v73
	v_cvt_pk_f16_f32 v78, v70, v71
	ds_write_b64 v149, v[78:79] offset:19456
	s_waitcnt vmcnt(16)
	v_cvt_pk_f16_f32 v79, v76, v77
	v_cvt_pk_f16_f32 v78, v74, v75
	s_and_saveexec_b64 s[12:13], s[8:9]
	ds_write_b64 v150, v[78:79] offset:19456
	s_or_b64 exec, exec, s[12:13]
	s_waitcnt vmcnt(10)
	v_cmp_lt_i32_e64 s[30:31], 1, v125
	v_cmp_lt_i32_e64 s[32:33], 1, v190
	v_cmp_lt_i32_e64 s[34:35], 1, v126
	v_cmp_lt_i32_e64 s[36:37], 1, v127
	v_cndmask_b32_e64 v191, 0, 1, s[30:31]
	v_cndmask_b32_e64 v190, 0, 2, s[32:33]
	v_cndmask_b32_e64 v126, 0, 4, s[34:35]
	v_cndmask_b32_e64 v127, 0, 8, s[36:37]
	v_or3_b32 v191, v191, v190, v126
	v_or_b32_e32 v191, v191, v127
	s_mov_b32 s26, 0x4b00
	s_mov_b32 s27, 0x5b00
	s_mov_b32 s28, 0x6b00
	buffer_load_dwordx4 v[2:5], v192, s[16:19], s26 offen nt
	buffer_load_dwordx4 v[14:17], v192, s[16:19], s26 offen offset:1024 nt
	buffer_load_dwordx4 v[34:37], v192, s[16:19], s26 offen offset:2048 nt
	buffer_load_dwordx4 v[46:49], v192, s[16:19], s26 offen offset:3072 nt
	buffer_load_dwordx4 v[54:57], v192, s[16:19], s27 offen nt
	buffer_load_dwordx4 v[58:61], v192, s[16:19], s27 offen offset:1024 nt
	buffer_load_dwordx4 v[62:65], v192, s[16:19], s27 offen offset:2048 nt
	buffer_load_dwordx4 v[66:69], v192, s[16:19], s27 offen offset:3072 nt
	buffer_load_dwordx4 v[70:73], v192, s[16:19], s28 offen nt
	buffer_load_dwordx4 v[74:77], v193, s[16:19], s26 offen offset:1024 nt
	s_mov_b32 s3, 0
	s_branch .LBB0_7
